# conversion groups by workgroup slot inside its XCD instead of by XCD (every XCD streams with 12/12/8 of its CUs at the three points of P1)
# speedup vs baseline: 1.0070x; 1.0070x over previous
.LBB0_202:
	s_bfe_u32 s53, s92, 0x30003
	s_cmpk_gt_u32 s92, 0xbf
	s_cselect_b64 s[0:1], -1, 0
	s_cmpk_eq_i32 s96, 0x100
	s_cselect_b64 s[6:7], -1, 0
	s_and_b64 s[2:3], s[6:7], exec
	s_movk_i32 s2, 0x5800
	v_writelane_b32 v253, s6, 48
	s_cselect_b32 s4, 0x600, 0
	s_cselect_b32 s50, s2, 0x6180
	s_cselect_b32 s95, 0x380, 0
	v_writelane_b32 v253, s7, 49
	s_and_b64 s[6:7], s[0:1], s[6:7]
	s_cmp_gt_u32 s53, 2
	s_mul_i32 s46, s94, s96
	s_cbranch_scc1 .LBB0_563
	s_lshl_b32 s20, s96, 3
	s_abs_i32 s18, s20
	s_waitcnt vmcnt(1)
	v_cvt_f32_u32_e32 v2, s18
	s_sub_i32 s0, 0, s18
	s_add_i32 s14, s20, s50
	s_lshl_b32 s23, s97, 3
	v_rcp_iflag_f32_e32 v2, v2
	s_add_i32 s14, s14, -1
	s_add_i32 s24, s23, s94
	s_abs_i32 s12, s14
	v_mul_f32_e32 v2, 0x4f7ffffe, v2
	v_cvt_u32_f32_e32 v2, v2
	s_nop 0
	v_readfirstlane_b32 s19, v2
	s_mul_i32 s0, s0, s19
	s_mul_hi_u32 s0, s19, s0
	s_add_i32 s19, s19, s0
	s_cmp_ge_i32 s24, s50
	s_mul_hi_u32 s13, s12, s19
	s_cbranch_scc1 .LBB0_211
	s_add_i32 s15, s24, 0xcc0
	s_cmpk_gt_i32 s24, 0xf7ff
	s_cbranch_scc0 .LBB0_212
	s_cmpk_gt_u32 s15, 0x5bf
	s_cbranch_scc0 .LBB0_213
	s_cmpk_gt_u32 s15, 0x6bf
	s_cbranch_scc0 .LBB0_214
	s_cmpk_gt_u32 s15, 0x8bf
	s_cbranch_scc0 .LBB0_215
	s_cmp_lt_u32 s24, 0xfffff340
	s_cbranch_scc0 .LBB0_216
	s_and_b32 s0, s24, 0xffff
	s_mul_i32 s0, s0, 0xaaab
	s_lshr_b32 s10, s0, 24
	s_mul_i32 s11, s10, 0xfffffe80
	s_add_i32 s11, s11, s24
	s_cmpk_gt_i32 s11, 0xff
	s_cbranch_scc0 .LBB0_217
	s_add_i32 s0, s11, 0xffffff00
	s_lshr_b32 s0, s0, 4
	v_readlane_b32 s56, v253, 31
	s_and_b32 s0, s0, 0xffffffe
	s_lshl_b32 s8, s10, 20
	s_lshl_b32 s2, s10, 22
	v_readlane_b32 s66, v253, 41
	v_readlane_b32 s67, v253, 42
	s_add_u32 s2, s66, s2
	s_addc_u32 s3, s67, 0
	s_mov_b32 s1, 0
	s_cmpk_lt_u32 s24, 0x6000
	s_cselect_b32 s9, s3, s85
	s_cselect_b32 s16, s2, s84
	s_lshl_b64 s[2:3], s[0:1], 19
	s_add_u32 s1, s16, s2
	s_addc_u32 s3, s9, s3
	s_lshl_b32 s2, s15, 6
	s_and_b32 s9, s2, 0x7c0
	s_lshl_b32 s2, s9, 2
	s_add_u32 s2, s1, s2
	s_addc_u32 s3, s3, 0
	s_lshl_b32 s1, s9, 9
	s_add_u32 s8, s90, s8
	s_addc_u32 s9, s91, 0
	s_add_u32 s1, s8, s1
	s_addc_u32 s8, s9, 0
	s_lshl_b32 s0, s0, 6
	s_add_u32 s0, s1, s0
	s_addc_u32 s1, s8, 0
	s_add_u32 s0, s0, 0x30c00000
	v_readlane_b32 s57, v253, 32
	v_readlane_b32 s58, v253, 33
	v_readlane_b32 s59, v253, 34
	v_readlane_b32 s60, v253, 35
	v_readlane_b32 s61, v253, 36
	v_readlane_b32 s62, v253, 37
	v_readlane_b32 s63, v253, 38
	v_readlane_b32 s64, v253, 39
	v_readlane_b32 s65, v253, 40
	v_readlane_b32 s68, v253, 43
	v_readlane_b32 s69, v253, 44
	v_readlane_b32 s70, v253, 45
	v_readlane_b32 s71, v253, 46
	s_addc_u32 s1, s1, 0
	s_mov_b64 s[8:9], 0
	s_branch .LBB0_218
